# c2 + hgrn pass-3 start-state prefix with 16-32 loads in flight (was one at a time), alignment-preserving pad
# baseline (speedup 1.0000x reference)
.LBB0_1999:
	s_and_b32 s60, s57, 7
	s_cmp_eq_u32 s60, 0
	s_cbranch_scc1 .LBB0_2004
	s_and_b32 s28, s57, -8
	v_mov_b32_e32 v2, 0
	v_mov_b32_e32 v3, v2
	v_mov_b32_e32 v4, v2
	v_mov_b32_e32 v5, v2
	v_mov_b32_e32 v6, v2
	v_mov_b32_e32 v7, v2
	v_mov_b32_e32 v8, v2
	v_mov_b32_e32 v9, v2
	v_mov_b32_e32 v10, v2
	v_mov_b32_e32 v11, v2
	v_mov_b32_e32 v12, v2
	v_mov_b32_e32 v13, v2
	v_mov_b32_e32 v14, v2
	v_mov_b32_e32 v15, v2
	v_mov_b32_e32 v16, v2
	v_mov_b32_e32 v17, v2
	v_mov_b32_e32 v18, v2
	v_mov_b32_e32 v19, v2
	v_mov_b32_e32 v20, v2
	v_mov_b32_e32 v21, v2
	v_mov_b32_e32 v22, v2
	v_mov_b32_e32 v23, v2
	v_mov_b32_e32 v24, v2
	v_mov_b32_e32 v25, v2
	v_mov_b32_e32 v26, v2
	v_mov_b32_e32 v27, v2
	v_mov_b32_e32 v28, v2
	v_mov_b32_e32 v29, v2
	v_mov_b32_e32 v30, v2
	v_mov_b32_e32 v31, v2
	v_mov_b32_e32 v32, v2
	v_mov_b32_e32 v33, v2
	s_mov_b32 s36, 0
	s_add_i32 s26, s28, s36
	s_ashr_i32 s27, s26, 31
	s_lshl_b64 s[42:43], s[26:27], 16
	v_lshl_add_u64 v[54:55], v[76:77], 0, s[42:43]
	s_lshl_b64 s[42:43], s[26:27], 9
	v_lshl_add_u64 v[56:57], v[82:83], 0, s[42:43]
	global_load_dwordx4 v[156:159], v[56:57], off
	global_load_dwordx4 v[160:163], v[54:55], off
	global_load_dwordx4 v[164:167], v[56:57], off offset:64
	global_load_dwordx4 v[168:171], v[54:55], off offset:16
	global_load_dwordx4 v[172:175], v[56:57], off offset:128
	global_load_dwordx4 v[176:179], v[54:55], off offset:32
	global_load_dwordx4 v[180:183], v[56:57], off offset:192
	global_load_dwordx4 v[184:187], v[54:55], off offset:48
	global_load_dwordx4 v[188:191], v[56:57], off offset:256
	global_load_dwordx4 v[192:195], v[54:55], off offset:64
	global_load_dwordx4 v[196:199], v[56:57], off offset:320
	global_load_dwordx4 v[200:203], v[54:55], off offset:80
	global_load_dwordx4 v[204:207], v[56:57], off offset:384
	global_load_dwordx4 v[208:211], v[54:55], off offset:96
	global_load_dwordx4 v[212:215], v[56:57], off offset:448
	global_load_dwordx4 v[216:219], v[54:55], off offset:112
.Lhgp_even:
	s_add_i32 s36, s36, 1
	s_cmp_eq_u32 s36, s60
	s_cbranch_scc1 .Lhgp_finA
	s_add_i32 s26, s28, s36
	s_ashr_i32 s27, s26, 31
	s_lshl_b64 s[42:43], s[26:27], 16
	v_lshl_add_u64 v[54:55], v[76:77], 0, s[42:43]
	s_lshl_b64 s[42:43], s[26:27], 9
	v_lshl_add_u64 v[56:57], v[82:83], 0, s[42:43]
	global_load_dwordx4 v[220:223], v[56:57], off
	global_load_dwordx4 v[224:227], v[54:55], off
	global_load_dwordx4 v[228:231], v[56:57], off offset:64
	global_load_dwordx4 v[232:235], v[54:55], off offset:16
	global_load_dwordx4 v[236:239], v[56:57], off offset:128
	global_load_dwordx4 v[240:243], v[54:55], off offset:32
	global_load_dwordx4 v[244:247], v[56:57], off offset:192
	global_load_dwordx4 v[248:251], v[54:55], off offset:48
	global_load_dwordx4 v[34:37], v[56:57], off offset:256
	global_load_dwordx4 v[38:41], v[54:55], off offset:64
	global_load_dwordx4 v[42:45], v[56:57], off offset:320
	global_load_dwordx4 v[46:49], v[54:55], off offset:80
	global_load_dwordx4 v[50:53], v[56:57], off offset:384
	global_load_dwordx4 v[58:61], v[54:55], off offset:96
	global_load_dwordx4 v[62:65], v[56:57], off offset:448
	global_load_dwordx4 v[66:69], v[54:55], off offset:112
	s_waitcnt vmcnt(30)
	v_pk_fma_f32 v[4:5], v[4:5], v[158:159], v[162:163]
	v_pk_fma_f32 v[2:3], v[2:3], v[156:157], v[160:161]
	s_waitcnt vmcnt(28)
	v_pk_fma_f32 v[8:9], v[8:9], v[166:167], v[170:171]
	v_pk_fma_f32 v[6:7], v[6:7], v[164:165], v[168:169]
	s_waitcnt vmcnt(26)
	v_pk_fma_f32 v[12:13], v[12:13], v[174:175], v[178:179]
	v_pk_fma_f32 v[10:11], v[10:11], v[172:173], v[176:177]
	s_waitcnt vmcnt(24)
	v_pk_fma_f32 v[16:17], v[16:17], v[182:183], v[186:187]
	v_pk_fma_f32 v[14:15], v[14:15], v[180:181], v[184:185]
	s_waitcnt vmcnt(22)
	v_pk_fma_f32 v[20:21], v[20:21], v[190:191], v[194:195]
	v_pk_fma_f32 v[18:19], v[18:19], v[188:189], v[192:193]
	s_waitcnt vmcnt(20)
	v_pk_fma_f32 v[24:25], v[24:25], v[198:199], v[202:203]
	v_pk_fma_f32 v[22:23], v[22:23], v[196:197], v[200:201]
	s_waitcnt vmcnt(18)
	v_pk_fma_f32 v[28:29], v[28:29], v[206:207], v[210:211]
	v_pk_fma_f32 v[26:27], v[26:27], v[204:205], v[208:209]
	s_waitcnt vmcnt(16)
	v_pk_fma_f32 v[32:33], v[32:33], v[214:215], v[218:219]
	v_pk_fma_f32 v[30:31], v[30:31], v[212:213], v[216:217]
	s_add_i32 s36, s36, 1
	s_cmp_eq_u32 s36, s60
	s_cbranch_scc1 .Lhgp_finB
	s_add_i32 s26, s28, s36
	s_ashr_i32 s27, s26, 31
	s_lshl_b64 s[42:43], s[26:27], 16
	v_lshl_add_u64 v[54:55], v[76:77], 0, s[42:43]
	s_lshl_b64 s[42:43], s[26:27], 9
	v_lshl_add_u64 v[56:57], v[82:83], 0, s[42:43]
	global_load_dwordx4 v[156:159], v[56:57], off
	global_load_dwordx4 v[160:163], v[54:55], off
	global_load_dwordx4 v[164:167], v[56:57], off offset:64
	global_load_dwordx4 v[168:171], v[54:55], off offset:16
	global_load_dwordx4 v[172:175], v[56:57], off offset:128
	global_load_dwordx4 v[176:179], v[54:55], off offset:32
	global_load_dwordx4 v[180:183], v[56:57], off offset:192
	global_load_dwordx4 v[184:187], v[54:55], off offset:48
	global_load_dwordx4 v[188:191], v[56:57], off offset:256
	global_load_dwordx4 v[192:195], v[54:55], off offset:64
	global_load_dwordx4 v[196:199], v[56:57], off offset:320
	global_load_dwordx4 v[200:203], v[54:55], off offset:80
	global_load_dwordx4 v[204:207], v[56:57], off offset:384
	global_load_dwordx4 v[208:211], v[54:55], off offset:96
	global_load_dwordx4 v[212:215], v[56:57], off offset:448
	global_load_dwordx4 v[216:219], v[54:55], off offset:112
	s_waitcnt vmcnt(30)
	v_pk_fma_f32 v[4:5], v[4:5], v[222:223], v[226:227]
	v_pk_fma_f32 v[2:3], v[2:3], v[220:221], v[224:225]
	s_waitcnt vmcnt(28)
	v_pk_fma_f32 v[8:9], v[8:9], v[230:231], v[234:235]
	v_pk_fma_f32 v[6:7], v[6:7], v[228:229], v[232:233]
	s_waitcnt vmcnt(26)
	v_pk_fma_f32 v[12:13], v[12:13], v[238:239], v[242:243]
	v_pk_fma_f32 v[10:11], v[10:11], v[236:237], v[240:241]
	s_waitcnt vmcnt(24)
	v_pk_fma_f32 v[16:17], v[16:17], v[246:247], v[250:251]
	v_pk_fma_f32 v[14:15], v[14:15], v[244:245], v[248:249]
	s_waitcnt vmcnt(22)
	v_pk_fma_f32 v[20:21], v[20:21], v[36:37], v[40:41]
	v_pk_fma_f32 v[18:19], v[18:19], v[34:35], v[38:39]
	s_waitcnt vmcnt(20)
	v_pk_fma_f32 v[24:25], v[24:25], v[44:45], v[48:49]
	v_pk_fma_f32 v[22:23], v[22:23], v[42:43], v[46:47]
	s_waitcnt vmcnt(18)
	v_pk_fma_f32 v[28:29], v[28:29], v[52:53], v[60:61]
	v_pk_fma_f32 v[26:27], v[26:27], v[50:51], v[58:59]
	s_waitcnt vmcnt(16)
	v_pk_fma_f32 v[32:33], v[32:33], v[64:65], v[68:69]
	v_pk_fma_f32 v[30:31], v[30:31], v[62:63], v[66:67]
	s_branch .Lhgp_even
.Lhgp_finA:
	s_waitcnt vmcnt(14)
	v_pk_fma_f32 v[4:5], v[4:5], v[158:159], v[162:163]
	v_pk_fma_f32 v[2:3], v[2:3], v[156:157], v[160:161]
	s_waitcnt vmcnt(12)
	v_pk_fma_f32 v[8:9], v[8:9], v[166:167], v[170:171]
	v_pk_fma_f32 v[6:7], v[6:7], v[164:165], v[168:169]
	s_waitcnt vmcnt(10)
	v_pk_fma_f32 v[12:13], v[12:13], v[174:175], v[178:179]
	v_pk_fma_f32 v[10:11], v[10:11], v[172:173], v[176:177]
	s_waitcnt vmcnt(8)
	v_pk_fma_f32 v[16:17], v[16:17], v[182:183], v[186:187]
	v_pk_fma_f32 v[14:15], v[14:15], v[180:181], v[184:185]
	s_waitcnt vmcnt(6)
	v_pk_fma_f32 v[20:21], v[20:21], v[190:191], v[194:195]
	v_pk_fma_f32 v[18:19], v[18:19], v[188:189], v[192:193]
	s_waitcnt vmcnt(4)
	v_pk_fma_f32 v[24:25], v[24:25], v[198:199], v[202:203]
	v_pk_fma_f32 v[22:23], v[22:23], v[196:197], v[200:201]
	s_waitcnt vmcnt(2)
	v_pk_fma_f32 v[28:29], v[28:29], v[206:207], v[210:211]
	v_pk_fma_f32 v[26:27], v[26:27], v[204:205], v[208:209]
	s_waitcnt vmcnt(0)
	v_pk_fma_f32 v[32:33], v[32:33], v[214:215], v[218:219]
	v_pk_fma_f32 v[30:31], v[30:31], v[212:213], v[216:217]
	s_branch .LBB0_2007
.Lhgp_finB:
	s_waitcnt vmcnt(14)
	v_pk_fma_f32 v[4:5], v[4:5], v[222:223], v[226:227]
	v_pk_fma_f32 v[2:3], v[2:3], v[220:221], v[224:225]
	s_waitcnt vmcnt(12)
	v_pk_fma_f32 v[8:9], v[8:9], v[230:231], v[234:235]
	v_pk_fma_f32 v[6:7], v[6:7], v[228:229], v[232:233]
	s_waitcnt vmcnt(10)
	v_pk_fma_f32 v[12:13], v[12:13], v[238:239], v[242:243]
	v_pk_fma_f32 v[10:11], v[10:11], v[236:237], v[240:241]
	s_waitcnt vmcnt(8)
	v_pk_fma_f32 v[16:17], v[16:17], v[246:247], v[250:251]
	v_pk_fma_f32 v[14:15], v[14:15], v[244:245], v[248:249]
	s_waitcnt vmcnt(6)
	v_pk_fma_f32 v[20:21], v[20:21], v[36:37], v[40:41]
	v_pk_fma_f32 v[18:19], v[18:19], v[34:35], v[38:39]
	s_waitcnt vmcnt(4)
	v_pk_fma_f32 v[24:25], v[24:25], v[44:45], v[48:49]
	v_pk_fma_f32 v[22:23], v[22:23], v[42:43], v[46:47]
	s_waitcnt vmcnt(2)
	v_pk_fma_f32 v[28:29], v[28:29], v[52:53], v[60:61]
	v_pk_fma_f32 v[26:27], v[26:27], v[50:51], v[58:59]
	s_waitcnt vmcnt(0)
	v_pk_fma_f32 v[32:33], v[32:33], v[64:65], v[68:69]
	v_pk_fma_f32 v[30:31], v[30:31], v[62:63], v[66:67]
	s_branch .LBB0_2007
	s_nop 0
	s_nop 0
	s_nop 0
	s_nop 0
	s_nop 0
	s_nop 0
	s_nop 0
	s_nop 0
	s_nop 0
	s_nop 0
	s_nop 0
.LBB0_2004:
	v_mov_b32_e32 v33, 0
	v_mov_b32_e32 v32, v33
	v_mov_b32_e32 v31, v33
	v_mov_b32_e32 v30, v33
	v_mov_b32_e32 v29, v33
	v_mov_b32_e32 v28, v33
	v_mov_b32_e32 v27, v33
	v_mov_b32_e32 v26, v33
	v_mov_b32_e32 v25, v33
	v_mov_b32_e32 v24, v33
	v_mov_b32_e32 v23, v33
	v_mov_b32_e32 v22, v33
	v_mov_b32_e32 v21, v33
	v_mov_b32_e32 v20, v33
	v_mov_b32_e32 v19, v33
	v_mov_b32_e32 v18, v33
	v_mov_b32_e32 v17, v33
	v_mov_b32_e32 v16, v33
	v_mov_b32_e32 v15, v33
	v_mov_b32_e32 v14, v33
	v_mov_b32_e32 v13, v33
	v_mov_b32_e32 v12, v33
	v_mov_b32_e32 v11, v33
	v_mov_b32_e32 v10, v33
	v_mov_b32_e32 v9, v33
	v_mov_b32_e32 v8, v33
	v_mov_b32_e32 v7, v33
	v_mov_b32_e32 v6, v33
	v_mov_b32_e32 v5, v33
	v_mov_b32_e32 v4, v33
	v_mov_b32_e32 v3, v33
	v_mov_b32_e32 v2, v33
	s_branch .LBB0_2007
.LBB0_2007:
	s_ashr_i32 s28, s57, 6
	s_ashr_i32 s29, s28, 31
	s_lshl_b32 s26, s60, 10
	s_lshl_b64 s[66:67], s[28:29], 13
	s_lshl_b32 s27, s57, 4
	s_or_b32 s66, s66, s26
	s_and_b32 s36, s27, 0x380
	s_lshl_b64 s[26:27], s[66:67], 11
	s_add_u32 s42, s4, s26
	s_addc_u32 s43, s5, s27
	s_lshl_b32 s61, s36, 1
	s_add_u32 s42, s42, s61
	s_addc_u32 s43, s43, 0
	s_add_u32 s58, s48, s26
	s_addc_u32 s59, s49, s27
	s_add_u32 s58, s58, s61
	s_addc_u32 s59, s59, 0
	s_add_u32 s26, s33, s26
	s_addc_u32 s27, s39, s27
	s_add_u32 s64, s26, s61
	s_addc_u32 s65, s27, 0
	v_lshl_add_u64 v[34:35], s[42:43], 0, v[94:95]
	v_lshl_add_u64 v[38:39], s[58:59], 0, v[94:95]
	global_load_dwordx2 v[36:37], v[34:35], off
	global_load_dwordx2 v[40:41], v[38:39], off
	v_lshl_add_u64 v[42:43], s[64:65], 0, v[94:95]
	global_load_dwordx2 v[44:45], v[42:43], off
	v_add_co_u32_e64 v34, s[26:27], s51, v34
	global_load_dword v144, v[84:85], off
	s_barrier
	v_addc_co_u32_e64 v35, s[26:27], 0, v35, s[26:27]
	s_mov_b32 s61, 0
	v_mov_b32_e32 v74, v116
	s_waitcnt vmcnt(2)
	ds_write2st64_b64 v110, v[36:37], v[40:41] offset0:66 offset1:74
	s_waitcnt vmcnt(1)
	ds_write_b64 v110, v[44:45] offset:41984
	global_load_dwordx2 v[96:97], v[34:35], off
	v_add_co_u32_e64 v34, s[26:27], s51, v38
	s_nop 1
	v_addc_co_u32_e64 v35, s[26:27], 0, v39, s[26:27]
	global_load_dwordx2 v[98:99], v[34:35], off
	v_add_co_u32_e64 v34, s[26:27], s51, v42
	s_nop 1
	v_addc_co_u32_e64 v35, s[26:27], 0, v43, s[26:27]
	global_load_dwordx2 v[100:101], v[34:35], off
	v_mov_b32_e32 v35, s67
	v_or_b32_e32 v34, s66, v78
	v_lshlrev_b64 v[36:37], 11, v[34:35]
	s_lshl_b32 s26, s57, 5
	v_lshl_add_u64 v[36:37], v[86:87], 0, v[36:37]
	s_and_b32 s26, s26, 0x700
	s_mov_b32 s27, s37
	v_lshl_add_u64 v[102:103], v[36:37], 0, s[26:27]
	s_movk_i32 s27, 0xc00
	v_mad_u64_u32 v[34:35], s[62:63], v34, s27, v[88:89]
	v_mad_i32_i24 v35, s67, v1, v35
	s_mul_i32 s63, s60, 0x300000
	v_lshl_add_u64 v[104:105], v[34:35], 0, s[36:37]
	s_mul_i32 s62, s28, 0x1800000
	s_or_b32 s36, s36, s63
	s_mul_hi_i32 s27, s28, 0x1800000
	s_add_u32 s62, s36, s62
	s_addc_u32 s63, 0, s27
	s_lshl_b32 s27, s60, 21
	s_lshl_b64 s[28:29], s[28:29], 24
	s_or_b32 s26, s26, s27
	s_or_b32 s28, s28, s26
	v_lshl_add_u64 v[106:107], s[62:63], 0, v[90:91]
	v_lshl_add_u64 v[108:109], s[28:29], 0, v[92:93]
	s_waitcnt lgkmcnt(0)
	s_barrier
	s_branch .LBB0_2009
